# P6c hoists its 8 partial-row + 8 scale loads to the row top (one round trip instead of eight); layer-loop grid barriers: waiting workgroups poll the cross-XCD release word directly, per-XCD release ad
# speedup vs baseline: 1.0402x; 1.0020x over previous
; __device__ __forceinline__ unsigned xb_ld(unsigned* p)              { return __hip_atomic_load(p, __ATOMIC_RELAXED, __HIP_MEMORY_SCOPE_AGENT); }
; __device__ __forceinline__ unsigned xb_add(unsigned* p, unsigned v) { return __hip_atomic_fetch_add(p, v, __ATOMIC_RELAXED, __HIP_MEMORY_SCOPE_AGENT); }
; #define XB_SPIN(cond, bar) do { unsigned _sp = 0; while (cond) { __builtin_amdgcn_s_sleep(1); \
;     if ((++_sp & 255u) == 0u) { if (xb_ld(&(bar)[XB_TMO])) break; if (_sp > XB_SPIN_CAP) { atomicAdd(&(bar)[XB_TMO], 1u); break; } } } } while (0)
; __device__ __forceinline__ void xcd_barrier(const XcdBarrier& b) {
;     ...
;         const unsigned old = xb_add(&bar[XB_XSUB(b.x)], 1u);
;         const unsigned gen = old / nloc;
;         if (old + 1u == (gen + 1u) * nloc) {
;             __builtin_amdgcn_fence(__ATOMIC_RELEASE, "agent");
;             asm volatile("s_waitcnt vmcnt(0)" ::: "memory");
;             const unsigned og = xb_add(&bar[XB_TOP], 1u);
;             const unsigned tg = og / nx;
;             if (og + 1u == (tg + 1u) * nx) xb_add(&bar[XB_TOPGEN], 1u);
;             else XB_SPIN(xb_ld(&bar[XB_TOPGEN]) == tg, bar);
;             __builtin_amdgcn_fence(__ATOMIC_ACQUIRE, "agent");
;             xb_add(&bar[XB_XGEN(b.x)], 1u);
;             asm volatile("s_waitcnt vmcnt(0)" ::: "memory");
;         } else {
;             XB_SPIN(xb_ld(&bar[XB_XGEN(b.x)]) == gen, bar);
.LBB0_251:
	s_or_b64 exec, exec, s[6:7]
	v_cvt_f32_u32_e32 v4, v2
	s_waitcnt vmcnt(0)
	v_readfirstlane_b32 s6, v3
	v_sub_u32_e32 v3, 0, v2
	v_rcp_iflag_f32_e32 v4, v4
	v_add_u32_e32 v5, s6, v1
	v_mul_f32_e32 v4, 0x4f7ffffe, v4
	v_cvt_u32_f32_e32 v4, v4
	v_mul_lo_u32 v1, v3, v4
	v_mul_hi_u32 v1, v4, v1
	v_add_u32_e32 v1, v4, v1
	v_mul_hi_u32 v1, v5, v1
	v_mul_lo_u32 v3, v1, v2
	v_sub_u32_e32 v3, v5, v3
	v_add_u32_e32 v4, 1, v1
	v_cmp_ge_u32_e32 vcc, v3, v2
	s_nop 1
	v_cndmask_b32_e32 v1, v1, v4, vcc
	v_sub_u32_e32 v4, v3, v2
	v_cndmask_b32_e32 v3, v3, v4, vcc
	v_add_u32_e32 v4, 1, v1
	v_cmp_ge_u32_e32 vcc, v3, v2
	v_add_u32_e32 v3, 1, v5
	s_nop 0
	v_cndmask_b32_e32 v1, v1, v4, vcc
	v_mul_lo_u32 v4, v2, v1
	v_add_u32_e32 v2, v4, v2
	v_cmp_ne_u32_e32 vcc, v3, v2
	s_and_saveexec_b64 s[6:7], vcc
	s_xor_b64 s[6:7], exec, s[6:7]
	s_cbranch_execz .LBB0_265
	v_readlane_b32 s8, v253, 11
	v_readlane_b32 s9, v253, 12
	s_waitcnt lgkmcnt(0)
	s_nop 3
	global_load_dword v0, v80, s[8:9] sc1
	s_waitcnt vmcnt(0)
	v_cmp_eq_u32_e32 vcc, v0, v1
	s_and_saveexec_b64 s[8:9], vcc
	s_cbranch_execz .LBB0_264
	s_mov_b32 s23, 1
	s_mov_b64 s[10:11], 0
	s_branch .LBB0_255

; __device__ __forceinline__ unsigned xb_ld(unsigned* p)              { return __hip_atomic_load(p, __ATOMIC_RELAXED, __HIP_MEMORY_SCOPE_AGENT); }
; #define XB_SPIN(cond, bar) do { unsigned _sp = 0; while (cond) { __builtin_amdgcn_s_sleep(1); \
;     if ((++_sp & 255u) == 0u) { if (xb_ld(&(bar)[XB_TMO])) break; if (_sp > XB_SPIN_CAP) { atomicAdd(&(bar)[XB_TMO], 1u); break; } } } } while (0)
; __device__ __forceinline__ void xcd_barrier(const XcdBarrier& b) {
;     ...
;             XB_SPIN(xb_ld(&bar[XB_XGEN(b.x)]) == gen, bar);
.LBB0_257:
	v_readlane_b32 s14, v253, 11
	v_readlane_b32 s15, v253, 12
	s_add_i32 s23, s23, 1
	s_mov_b64 s[16:17], -1
	s_nop 2
	global_load_dword v0, v80, s[14:15] sc1
	s_waitcnt vmcnt(0)
	v_cmp_ne_u32_e32 vcc, v0, v1
	s_orn2_b64 s[14:15], vcc, exec
	s_branch .LBB0_254

; __device__ __forceinline__ unsigned xb_ld(unsigned* p)              { return __hip_atomic_load(p, __ATOMIC_RELAXED, __HIP_MEMORY_SCOPE_AGENT); }
; __device__ __forceinline__ unsigned xb_add(unsigned* p, unsigned v) { return __hip_atomic_fetch_add(p, v, __ATOMIC_RELAXED, __HIP_MEMORY_SCOPE_AGENT); }
; #define XB_SPIN(cond, bar) do { unsigned _sp = 0; while (cond) { __builtin_amdgcn_s_sleep(1); \
;     if ((++_sp & 255u) == 0u) { if (xb_ld(&(bar)[XB_TMO])) break; if (_sp > XB_SPIN_CAP) { atomicAdd(&(bar)[XB_TMO], 1u); break; } } } } while (0)
; __device__ __forceinline__ void xcd_barrier(const XcdBarrier& b) {
;     ...
;             __builtin_amdgcn_fence(__ATOMIC_RELEASE, "agent");
;             asm volatile("s_waitcnt vmcnt(0)" ::: "memory");
;             const unsigned og = xb_add(&bar[XB_TOP], 1u);
;             const unsigned tg = og / nx;
;             if (og + 1u == (tg + 1u) * nx) xb_add(&bar[XB_TOPGEN], 1u);
;             else XB_SPIN(xb_ld(&bar[XB_TOPGEN]) == tg, bar);
;             __builtin_amdgcn_fence(__ATOMIC_ACQUIRE, "agent");
;             xb_add(&bar[XB_XGEN(b.x)], 1u);
;             asm volatile("s_waitcnt vmcnt(0)" ::: "memory");
.LBB0_282:
	s_or_b64 exec, exec, s[6:7]
	s_mov_b64 s[6:7], exec
	v_mbcnt_lo_u32_b32 v0, s6, 0
	v_mbcnt_hi_u32_b32 v0, s7, v0
	v_cmp_eq_u32_e32 vcc, 0, v0
	s_waitcnt vmcnt(0)
	s_and_saveexec_b64 s[8:9], vcc
	s_cbranch_execz .LBB0_284
	s_bcnt1_i32_b64 s6, s[6:7]
	v_mov_b32_e32 v0, s6
	v_readlane_b32 s6, v253, 7
	v_readlane_b32 s7, v253, 8
	s_nop 4
	s_nop 0

; __device__ __forceinline__ void row_peer_reduce(const Params& P, unsigned char* ws, int l, int rowi, int lane, float* __restrict__ xout) {
;     const size_t n = (size_t)rowi; const bf16* Z = (const bf16*)(ws + WS_Z); const unsigned char* PARTQ = ws + WS_PART; const float* PSCL = (const float*)(ws + WS_PSCL);
;     const f2 st = *(const f2*)((const float*)(ws + WS_X1) + 2 * n);
;     const float* g1 = P.in[16] + (size_t)l * D; const float* b1 = P.in[17] + (size_t)l * D;
;     float acc[32];
; #pragma unroll
;     for (int j = 0; j < 2; ++j)
; #pragma unroll
;         for (int q = 0; q < 4; ++q) { const int col = 1024 * j + 16 * lane + 4 * q; const u2 zw = *(const u2*)(Z + n * D + col); const f4 a = mk_f4(__uint_as_float(zw.x << 16), __uint_as_float(zw.x & 0xffff0000u), __uint_as_float(zw.y << 16), __uint_as_float(zw.y & 0xffff0000u)), gg = *(const f4*)(g1 + col), bb = *(const f4*)(b1 + col);
;             acc[16 * j + 4 * q] = ALPHA * ((a.x - st.x) * st.y * gg.x + bb.x); acc[16 * j + 4 * q + 1] = ALPHA * ((a.y - st.x) * st.y * gg.y + bb.y);
;             acc[16 * j + 4 * q + 2] = ALPHA * ((a.z - st.x) * st.y * gg.z + bb.z); acc[16 * j + 4 * q + 3] = ALPHA * ((a.w - st.x) * st.y * gg.w + bb.w); }
; #pragma unroll 4
;     for (int xb_ = 0; xb_ < 8; ++xb_) { const u4 a = *(const u4*)(PARTQ + ((size_t)xb_ * NTOK + ((n + 5u * (unsigned)xb_) & (size_t)(NTOK - 1))) * 1024u + (unsigned)(16 * lane)); const float psc = PSCL[(size_t)xb_ * NTOK + n];
; #pragma unroll
.LBB0_1592:
	s_add_u32 s26, s92, 0x5b000000
	s_addc_u32 s27, s93, 0
	s_add_u32 s28, s92, 0x64000000
	s_addc_u32 s29, s93, 0
	s_and_b32 s22, s6, 0x1fff
	s_lshl_b32 s22, s22, 10
	v_add_u32_e32 v144, s22, v32
	global_load_dwordx4 v[104:107], v144, s[26:27]
	s_lshl_b32 s23, s6, 2
	v_mov_b32_e32 v176, s23
	global_load_dword v136, v176, s[28:29]
	s_add_i32 s22, s6, 5
	s_and_b32 s22, s22, 0x1fff
	s_lshl_b32 s22, s22, 10
	s_add_i32 s22, s22, 0x800000
	v_add_u32_e32 v145, s22, v32
	global_load_dwordx4 v[108:111], v145, s[26:27]
	s_add_i32 s23, s6, 0x2000
	s_lshl_b32 s23, s23, 2
	v_mov_b32_e32 v177, s23
	global_load_dword v137, v177, s[28:29]
	s_add_i32 s22, s6, 10
	s_and_b32 s22, s22, 0x1fff
	s_lshl_b32 s22, s22, 10
	s_add_i32 s22, s22, 0x1000000
	v_add_u32_e32 v146, s22, v32
	global_load_dwordx4 v[112:115], v146, s[26:27]
	s_add_i32 s23, s6, 0x4000
	s_lshl_b32 s23, s23, 2
	v_mov_b32_e32 v178, s23
	global_load_dword v138, v178, s[28:29]
	s_add_i32 s22, s6, 15
	s_and_b32 s22, s22, 0x1fff
	s_lshl_b32 s22, s22, 10
	s_add_i32 s22, s22, 0x1800000
	v_add_u32_e32 v147, s22, v32
	global_load_dwordx4 v[116:119], v147, s[26:27]
	s_add_i32 s23, s6, 0x6000
	s_lshl_b32 s23, s23, 2
	v_mov_b32_e32 v179, s23
	global_load_dword v139, v179, s[28:29]
	s_add_i32 s22, s6, 20
	s_and_b32 s22, s22, 0x1fff
	s_lshl_b32 s22, s22, 10
	s_add_i32 s22, s22, 0x2000000
	v_add_u32_e32 v148, s22, v32
	global_load_dwordx4 v[120:123], v148, s[26:27]
	s_add_i32 s23, s6, 0x8000
	s_lshl_b32 s23, s23, 2
	v_mov_b32_e32 v180, s23
	global_load_dword v140, v180, s[28:29]
	s_add_i32 s22, s6, 25
	s_and_b32 s22, s22, 0x1fff
	s_lshl_b32 s22, s22, 10
	s_add_i32 s22, s22, 0x2800000
	v_add_u32_e32 v149, s22, v32
	global_load_dwordx4 v[124:127], v149, s[26:27]
	s_add_i32 s23, s6, 0xa000
	s_lshl_b32 s23, s23, 2
	v_mov_b32_e32 v181, s23
	global_load_dword v141, v181, s[28:29]
	s_add_i32 s22, s6, 30
	s_and_b32 s22, s22, 0x1fff
	s_lshl_b32 s22, s22, 10
	s_add_i32 s22, s22, 0x3000000
	v_add_u32_e32 v150, s22, v32
	global_load_dwordx4 v[128:131], v150, s[26:27]
	s_add_i32 s23, s6, 0xc000
	s_lshl_b32 s23, s23, 2
	v_mov_b32_e32 v182, s23
	global_load_dword v142, v182, s[28:29]
	s_add_i32 s22, s6, 35
	s_and_b32 s22, s22, 0x1fff
	s_lshl_b32 s22, s22, 10
	s_add_i32 s22, s22, 0x3800000
	v_add_u32_e32 v151, s22, v32
	global_load_dwordx4 v[132:135], v151, s[26:27]
	s_add_i32 s23, s6, 0xe000
	s_lshl_b32 s23, s23, 2
	v_mov_b32_e32 v183, s23
	global_load_dword v143, v183, s[28:29]
	s_ashr_i32 s7, s6, 31
	s_lshl_b64 s[4:5], s[6:7], 3
	s_add_u32 s4, s38, s4
	s_addc_u32 s5, s39, s5
	global_load_dwordx2 v[74:75], v80, s[4:5]
	s_lshl_b64 s[12:13], s[6:7], 12
	v_lshl_add_u64 v[4:5], v[52:53], 0, s[12:13]
	global_load_dwordx4 v[0:3], v[4:5], off offset:16
	global_load_dwordx4 v[6:9], v[4:5], off
	global_load_dwordx4 v[10:13], v[34:35], off offset:48
	global_load_dwordx4 v[14:17], v[34:35], off offset:32
	global_load_dwordx4 v[18:21], v[34:35], off offset:16
	global_load_dwordx4 v[22:25], v[34:35], off
	global_load_dwordx4 v[26:29], v[36:37], off offset:48
	global_load_dwordx4 v[64:67], v[36:37], off offset:32
	global_load_dwordx4 v[60:63], v[36:37], off offset:16
	global_load_dwordx4 v[56:59], v[36:37], off
	s_mov_b32 s4, 0x3fd744fd
	s_mov_b64 s[14:15], 0x4000
	s_mov_b64 s[16:17], 0x2000
	s_mov_b64 s[18:19], 0
	s_mov_b32 s47, s46
	s_mov_b32 s48, s45
	s_mov_b32 s49, s44
	s_mov_b32 s50, s43
	s_mov_b64 s[34:35], 0
	s_waitcnt vmcnt(0)
	v_lshlrev_b32_e32 v30, 16, v6
	v_and_b32_e32 v31, 0xffff0000, v6
	v_lshlrev_b32_e32 v6, 16, v7
	v_and_b32_e32 v7, 0xffff0000, v7
	v_pk_add_f32 v[6:7], v[6:7], v[74:75] op_sel_hi:[1,0] neg_lo:[0,1] neg_hi:[0,1]
	s_nop 0
	v_pk_mul_f32 v[6:7], v[74:75], v[6:7] op_sel:[1,0]
	v_pk_add_f32 v[30:31], v[30:31], v[74:75] op_sel_hi:[1,0] neg_lo:[0,1] neg_hi:[0,1]
	v_pk_fma_f32 v[6:7], v[24:25], v[6:7], v[58:59]
	v_pk_mul_f32 v[30:31], v[74:75], v[30:31] op_sel:[1,0]
	v_pk_mul_f32 v[58:59], v[6:7], s[4:5] op_sel_hi:[1,0]
	v_lshlrev_b32_e32 v6, 16, v8
	v_and_b32_e32 v7, 0xffff0000, v8
	v_pk_add_f32 v[6:7], v[6:7], v[74:75] op_sel_hi:[1,0] neg_lo:[0,1] neg_hi:[0,1]
	v_pk_fma_f32 v[22:23], v[22:23], v[30:31], v[56:57]
	v_pk_mul_f32 v[6:7], v[74:75], v[6:7] op_sel:[1,0]
	v_pk_mul_f32 v[56:57], v[22:23], s[4:5] op_sel_hi:[1,0]
	v_pk_fma_f32 v[6:7], v[18:19], v[6:7], v[60:61]
	s_nop 0
	v_pk_mul_f32 v[60:61], v[6:7], s[4:5] op_sel_hi:[1,0]
	v_lshlrev_b32_e32 v6, 16, v9
	v_and_b32_e32 v7, 0xffff0000, v9
	v_pk_add_f32 v[6:7], v[6:7], v[74:75] op_sel_hi:[1,0] neg_lo:[0,1] neg_hi:[0,1]
	s_nop 0
	v_pk_mul_f32 v[6:7], v[74:75], v[6:7] op_sel:[1,0]
	s_nop 0
	v_pk_fma_f32 v[6:7], v[20:21], v[6:7], v[62:63]
	s_nop 0
	v_pk_mul_f32 v[62:63], v[6:7], s[4:5] op_sel_hi:[1,0]
	v_lshlrev_b32_e32 v6, 16, v0
	v_and_b32_e32 v7, 0xffff0000, v0
	v_lshlrev_b32_e32 v0, 16, v1
	v_and_b32_e32 v1, 0xffff0000, v1
	v_pk_add_f32 v[0:1], v[0:1], v[74:75] op_sel_hi:[1,0] neg_lo:[0,1] neg_hi:[0,1]
	v_pk_add_f32 v[6:7], v[6:7], v[74:75] op_sel_hi:[1,0] neg_lo:[0,1] neg_hi:[0,1]
	v_pk_mul_f32 v[0:1], v[74:75], v[0:1] op_sel:[1,0]
	v_pk_mul_f32 v[6:7], v[74:75], v[6:7] op_sel:[1,0]
	v_pk_fma_f32 v[0:1], v[16:17], v[0:1], v[66:67]
	v_pk_fma_f32 v[6:7], v[14:15], v[6:7], v[64:65]
	v_pk_mul_f32 v[66:67], v[0:1], s[4:5] op_sel_hi:[1,0]
	v_lshlrev_b32_e32 v0, 16, v2
	v_and_b32_e32 v1, 0xffff0000, v2
	v_pk_add_f32 v[0:1], v[0:1], v[74:75] op_sel_hi:[1,0] neg_lo:[0,1] neg_hi:[0,1]
	v_pk_mul_f32 v[64:65], v[6:7], s[4:5] op_sel_hi:[1,0]
	v_pk_mul_f32 v[0:1], v[74:75], v[0:1] op_sel:[1,0]
	s_nop 0
	v_pk_fma_f32 v[0:1], v[10:11], v[0:1], v[26:27]
	s_nop 0
	v_pk_mul_f32 v[68:69], v[0:1], s[4:5] op_sel_hi:[1,0]
	v_lshlrev_b32_e32 v0, 16, v3
	v_and_b32_e32 v1, 0xffff0000, v3
	v_pk_add_f32 v[0:1], v[0:1], v[74:75] op_sel_hi:[1,0] neg_lo:[0,1] neg_hi:[0,1]
	s_nop 0
	v_pk_mul_f32 v[0:1], v[74:75], v[0:1] op_sel:[1,0]
	s_nop 0
	v_pk_fma_f32 v[0:1], v[12:13], v[0:1], v[28:29]
	s_nop 0
	v_pk_mul_f32 v[70:71], v[0:1], s[4:5] op_sel_hi:[1,0]
	global_load_dwordx4 v[0:3], v[4:5], off offset:2064
	global_load_dwordx4 v[28:31], v[4:5], off offset:2048
	s_nop 0
	global_load_dwordx4 v[4:7], v[38:39], off offset:48
	global_load_dwordx4 v[12:15], v[38:39], off offset:32
	global_load_dwordx4 v[20:23], v[38:39], off offset:16
	global_load_dwordx4 v[82:85], v[38:39], off
	global_load_dwordx4 v[8:11], v[40:41], off offset:48
	global_load_dwordx4 v[16:19], v[40:41], off offset:32
	global_load_dwordx4 v[24:27], v[40:41], off offset:16
	global_load_dwordx4 v[86:89], v[40:41], off
	s_waitcnt vmcnt(8)
; __device__ __forceinline__ void row_peer_reduce(const Params& P, unsigned char* ws, int l, int rowi, int lane, float* __restrict__ xout) {
;     ...
;         for (int q = 0; q < 4; ++q) { const int col = 1024 * j + 16 * lane + 4 * q; const u2 zw = *(const u2*)(Z + n * D + col); const f4 a = mk_f4(__uint_as_float(zw.x << 16), __uint_as_float(zw.x & 0xffff0000u), __uint_as_float(zw.y << 16), __uint_as_float(zw.y & 0xffff0000u)), gg = *(const f4*)(g1 + col), bb = *(const f4*)(b1 + col);
;             acc[16 * j + 4 * q] = ALPHA * ((a.x - st.x) * st.y * gg.x + bb.x); acc[16 * j + 4 * q + 1] = ALPHA * ((a.y - st.x) * st.y * gg.y + bb.y);
;             acc[16 * j + 4 * q + 2] = ALPHA * ((a.z - st.x) * st.y * gg.z + bb.z); acc[16 * j + 4 * q + 3] = ALPHA * ((a.w - st.x) * st.y * gg.w + bb.w); }
; #pragma unroll 4
;     for (int xb_ = 0; xb_ < 8; ++xb_) { const u4 a = *(const u4*)(PARTQ + ((size_t)xb_ * NTOK + ((n + 5u * (unsigned)xb_) & (size_t)(NTOK - 1))) * 1024u + (unsigned)(16 * lane)); const float psc = PSCL[(size_t)xb_ * NTOK + n];
; #pragma unroll
;         for (int d = 0; d < 4; ++d) { const f2 p0 = __builtin_amdgcn_cvt_scalef32_pk_f32_fp4(a[d], 1.0f, 0), p1 = __builtin_amdgcn_cvt_scalef32_pk_f32_fp4(a[d], 1.0f, 1), p2 = __builtin_amdgcn_cvt_scalef32_pk_f32_fp4(a[d], 1.0f, 2), p3 = __builtin_amdgcn_cvt_scalef32_pk_f32_fp4(a[d], 1.0f, 3);
;             const int o = 16 * (d >> 1) + 8 * (d & 1);
;             acc[o] += psc * p0.x; acc[o + 1] += psc * p0.y; acc[o + 2] += psc * p1.x; acc[o + 3] += psc * p1.y; acc[o + 4] += psc * p2.x; acc[o + 5] += psc * p2.y; acc[o + 6] += psc * p3.x; acc[o + 7] += psc * p3.y; } }
	v_lshlrev_b32_e32 v72, 16, v28
	v_and_b32_e32 v73, 0xffff0000, v28
	v_pk_add_f32 v[72:73], v[72:73], v[74:75] op_sel_hi:[1,0] neg_lo:[0,1] neg_hi:[0,1]
	v_lshlrev_b32_e32 v28, 16, v29
	v_pk_mul_f32 v[72:73], v[74:75], v[72:73] op_sel:[1,0]
	v_and_b32_e32 v29, 0xffff0000, v29
	v_pk_add_f32 v[28:29], v[28:29], v[74:75] op_sel_hi:[1,0] neg_lo:[0,1] neg_hi:[0,1]
	s_waitcnt vmcnt(0)
	v_pk_fma_f32 v[72:73], v[82:83], v[72:73], v[86:87]
	v_lshlrev_b32_e32 v82, 16, v30
	v_and_b32_e32 v83, 0xffff0000, v30
	v_pk_add_f32 v[82:83], v[82:83], v[74:75] op_sel_hi:[1,0] neg_lo:[0,1] neg_hi:[0,1]
	v_pk_mul_f32 v[28:29], v[74:75], v[28:29] op_sel:[1,0]
	v_pk_mul_f32 v[82:83], v[74:75], v[82:83] op_sel:[1,0]
	v_pk_fma_f32 v[28:29], v[84:85], v[28:29], v[88:89]
	v_pk_fma_f32 v[20:21], v[20:21], v[82:83], v[24:25]
	v_lshlrev_b32_e32 v24, 16, v31
	v_and_b32_e32 v25, 0xffff0000, v31
	v_pk_add_f32 v[24:25], v[24:25], v[74:75] op_sel_hi:[1,0] neg_lo:[0,1] neg_hi:[0,1]
	v_pk_mul_f32 v[72:73], v[72:73], s[4:5] op_sel_hi:[1,0]
	v_pk_mul_f32 v[24:25], v[74:75], v[24:25] op_sel:[1,0]
	v_pk_mul_f32 v[28:29], v[28:29], s[4:5] op_sel_hi:[1,0]
	v_pk_fma_f32 v[22:23], v[22:23], v[24:25], v[26:27]
	v_lshlrev_b32_e32 v24, 16, v0
	v_and_b32_e32 v25, 0xffff0000, v0
	v_lshlrev_b32_e32 v0, 16, v1
	v_and_b32_e32 v1, 0xffff0000, v1
	v_pk_add_f32 v[0:1], v[0:1], v[74:75] op_sel_hi:[1,0] neg_lo:[0,1] neg_hi:[0,1]
	v_pk_add_f32 v[24:25], v[24:25], v[74:75] op_sel_hi:[1,0] neg_lo:[0,1] neg_hi:[0,1]
	v_pk_mul_f32 v[0:1], v[74:75], v[0:1] op_sel:[1,0]
	v_pk_mul_f32 v[24:25], v[74:75], v[24:25] op_sel:[1,0]
	v_pk_fma_f32 v[0:1], v[14:15], v[0:1], v[18:19]
	v_lshlrev_b32_e32 v14, 16, v2
	v_and_b32_e32 v15, 0xffff0000, v2
	v_lshlrev_b32_e32 v2, 16, v3
	v_and_b32_e32 v3, 0xffff0000, v3
	v_pk_add_f32 v[14:15], v[14:15], v[74:75] op_sel_hi:[1,0] neg_lo:[0,1] neg_hi:[0,1]
	v_pk_add_f32 v[2:3], v[2:3], v[74:75] op_sel_hi:[1,0] neg_lo:[0,1] neg_hi:[0,1]
	v_pk_mul_f32 v[14:15], v[74:75], v[14:15] op_sel:[1,0]
	v_pk_mul_f32 v[2:3], v[74:75], v[2:3] op_sel:[1,0]
	v_pk_fma_f32 v[12:13], v[12:13], v[24:25], v[16:17]
	v_pk_fma_f32 v[4:5], v[4:5], v[14:15], v[8:9]
	v_pk_fma_f32 v[2:3], v[6:7], v[2:3], v[10:11]
	v_pk_mul_f32 v[20:21], v[20:21], s[4:5] op_sel_hi:[1,0]
	v_pk_mul_f32 v[22:23], v[22:23], s[4:5] op_sel_hi:[1,0]
	v_pk_mul_f32 v[12:13], v[12:13], s[4:5] op_sel_hi:[1,0]
	v_pk_mul_f32 v[0:1], v[0:1], s[4:5] op_sel_hi:[1,0]
	v_pk_mul_f32 v[4:5], v[4:5], s[4:5] op_sel_hi:[1,0]
	v_pk_mul_f32 v[2:3], v[2:3], s[4:5] op_sel_hi:[1,0]
	s_mov_b64 s[4:5], 0x6000
.LBB0_1593:
	s_cmp_eq_u32 s34, 0
	s_cbranch_scc0 .Lp6c_set1
	v_mov_b64_e32 v[156:157], v[104:105]
	v_mov_b64_e32 v[158:159], v[106:107]
	v_mov_b32_e32 v172, v136
	v_mov_b64_e32 v[160:161], v[108:109]
	v_mov_b64_e32 v[162:163], v[110:111]
	v_mov_b32_e32 v173, v137
	v_mov_b64_e32 v[164:165], v[112:113]
	v_mov_b64_e32 v[166:167], v[114:115]
	v_mov_b32_e32 v174, v138
	v_mov_b64_e32 v[168:169], v[116:117]
	v_mov_b64_e32 v[170:171], v[118:119]
	v_mov_b32_e32 v175, v139
	s_branch .Lp6c_join
.Lp6c_set1:
	v_mov_b64_e32 v[156:157], v[120:121]
	v_mov_b64_e32 v[158:159], v[122:123]
	v_mov_b32_e32 v172, v140
	v_mov_b64_e32 v[160:161], v[124:125]
	v_mov_b64_e32 v[162:163], v[126:127]
	v_mov_b32_e32 v173, v141
	v_mov_b64_e32 v[164:165], v[128:129]
	v_mov_b64_e32 v[166:167], v[130:131]
	v_mov_b32_e32 v174, v142
	v_mov_b64_e32 v[168:169], v[132:133]
	v_mov_b64_e32 v[170:171], v[134:135]
	v_mov_b32_e32 v175, v143
.Lp6c_join:
	s_and_b32 s22, s50, 0x1fff
	s_add_u32 s26, s4, s22
	s_addc_u32 s27, s5, 0
	s_and_b32 s22, s49, 0x1fff
	s_add_u32 s28, s14, s22
	s_addc_u32 s29, s15, 0
	s_and_b32 s22, s48, 0x1fff
	s_add_u32 s30, s16, s22
	s_addc_u32 s31, s17, 0
	s_and_b32 s22, s47, 0x1fff
	s_add_u32 s22, s18, s22
	s_addc_u32 s23, s19, 0
	s_lshl_b64 s[22:23], s[22:23], 10
	s_add_u32 s22, s41, s34
	v_mov_b64_e32 v[6:7], v[156:157]
	v_mov_b64_e32 v[8:9], v[158:159]
	s_addc_u32 s23, s42, s35
	v_mov_b32_e32 v10, v172
	s_lshl_b64 s[30:31], s[30:31], 10
	s_lshl_b64 s[28:29], s[28:29], 10
	s_lshl_b64 s[26:27], s[26:27], 10
	s_add_u32 s34, s34, 0x20000
	s_addc_u32 s35, s35, 0
	s_add_u32 s4, s4, 0x8000
	s_addc_u32 s5, s5, 0
	s_add_i32 s50, s50, 20
	s_add_u32 s14, s14, 0x8000
	s_addc_u32 s15, s15, 0
	s_add_i32 s49, s49, 20
	s_add_u32 s16, s16, 0x8000
	s_addc_u32 s17, s17, 0
	s_add_i32 s48, s48, 20
	s_add_u32 s18, s18, 0x8000
	s_addc_u32 s19, s19, 0
	s_add_i32 s47, s47, 20
	s_cmp_eq_u32 s34, 0x40000
	s_nop 0
	v_cvt_scalef32_pk_f32_fp4 v[18:19], v6, 1.0 op_sel:[0,1,0]
	v_cvt_scalef32_pk_f32_fp4 v[24:25], v6, 1.0 op_sel:[1,1,0]
	s_nop 0
	v_pk_fma_f32 v[18:19], v[10:11], v[18:19], v[60:61] op_sel_hi:[0,1,1]
	v_pk_fma_f32 v[24:25], v[10:11], v[24:25], v[62:63] op_sel_hi:[0,1,1]
	v_cvt_scalef32_pk_f32_fp4 v[26:27], v7, 1.0
	v_cvt_scalef32_pk_f32_fp4 v[60:61], v8, 1.0 op_sel:[1,0,0]
	v_cvt_scalef32_pk_f32_fp4 v[62:63], v8, 1.0 op_sel:[0,1,0]
	v_cvt_scalef32_pk_f32_fp4 v[14:15], v6, 1.0
	v_cvt_scalef32_pk_f32_fp4 v[16:17], v6, 1.0 op_sel:[1,0,0]
	v_pk_fma_f32 v[26:27], v[10:11], v[26:27], v[64:65] op_sel_hi:[0,1,1]
	v_cvt_scalef32_pk_f32_fp4 v[64:65], v8, 1.0 op_sel:[1,1,0]
	v_pk_fma_f32 v[28:29], v[10:11], v[60:61], v[28:29] op_sel_hi:[0,1,1]
	v_pk_fma_f32 v[20:21], v[10:11], v[62:63], v[20:21] op_sel_hi:[0,1,1]
	v_cvt_scalef32_pk_f32_fp4 v[60:61], v9, 1.0
	v_cvt_scalef32_pk_f32_fp4 v[62:63], v9, 1.0 op_sel:[1,0,0]
	v_pk_fma_f32 v[14:15], v[10:11], v[14:15], v[56:57] op_sel_hi:[0,1,1]
	v_pk_fma_f32 v[16:17], v[10:11], v[16:17], v[58:59] op_sel_hi:[0,1,1]
	v_cvt_scalef32_pk_f32_fp4 v[30:31], v7, 1.0 op_sel:[1,0,0]
	v_cvt_scalef32_pk_f32_fp4 v[56:57], v7, 1.0 op_sel:[0,1,0]
; __device__ __forceinline__ void row_peer_reduce(const Params& P, unsigned char* ws, int l, int rowi, int lane, float* __restrict__ xout) {
;     ...
;     for (int xb_ = 0; xb_ < 8; ++xb_) { const u4 a = *(const u4*)(PARTQ + ((size_t)xb_ * NTOK + ((n + 5u * (unsigned)xb_) & (size_t)(NTOK - 1))) * 1024u + (unsigned)(16 * lane)); const float psc = PSCL[(size_t)xb_ * NTOK + n];
; #pragma unroll
;         for (int d = 0; d < 4; ++d) { const f2 p0 = __builtin_amdgcn_cvt_scalef32_pk_f32_fp4(a[d], 1.0f, 0), p1 = __builtin_amdgcn_cvt_scalef32_pk_f32_fp4(a[d], 1.0f, 1), p2 = __builtin_amdgcn_cvt_scalef32_pk_f32_fp4(a[d], 1.0f, 2), p3 = __builtin_amdgcn_cvt_scalef32_pk_f32_fp4(a[d], 1.0f, 3);
;             const int o = 16 * (d >> 1) + 8 * (d & 1);
;             acc[o] += psc * p0.x; acc[o + 1] += psc * p0.y; acc[o + 2] += psc * p1.x; acc[o + 3] += psc * p1.y; acc[o + 4] += psc * p2.x; acc[o + 5] += psc * p2.y; acc[o + 6] += psc * p3.x; acc[o + 7] += psc * p3.y; } }
	v_cvt_scalef32_pk_f32_fp4 v[6:7], v7, 1.0 op_sel:[1,1,0]
	v_cvt_scalef32_pk_f32_fp4 v[58:59], v8, 1.0
	v_pk_fma_f32 v[22:23], v[10:11], v[64:65], v[22:23] op_sel_hi:[0,1,1]
	v_cvt_scalef32_pk_f32_fp4 v[64:65], v9, 1.0 op_sel:[0,1,0]
	v_cvt_scalef32_pk_f32_fp4 v[8:9], v9, 1.0 op_sel:[1,1,0]
	v_pk_fma_f32 v[12:13], v[10:11], v[60:61], v[12:13] op_sel_hi:[0,1,1]
	v_pk_fma_f32 v[60:61], v[10:11], v[62:63], v[0:1] op_sel_hi:[0,1,1]
	v_pk_fma_f32 v[30:31], v[10:11], v[30:31], v[66:67] op_sel_hi:[0,1,1]
	v_pk_fma_f32 v[56:57], v[10:11], v[56:57], v[68:69] op_sel_hi:[0,1,1]
	v_pk_fma_f32 v[6:7], v[10:11], v[6:7], v[70:71] op_sel_hi:[0,1,1]
	v_pk_fma_f32 v[58:59], v[10:11], v[58:59], v[72:73] op_sel_hi:[0,1,1]
	v_pk_fma_f32 v[4:5], v[10:11], v[64:65], v[4:5] op_sel_hi:[0,1,1]
	v_pk_fma_f32 v[8:9], v[10:11], v[8:9], v[2:3] op_sel_hi:[0,1,1]
	v_mov_b64_e32 v[0:1], v[160:161]
	v_mov_b64_e32 v[2:3], v[162:163]
	s_nop 0
	v_mov_b32_e32 v10, v173
	s_nop 0
	v_cvt_scalef32_pk_f32_fp4 v[62:63], v0, 1.0
	v_cvt_scalef32_pk_f32_fp4 v[64:65], v0, 1.0 op_sel:[1,0,0]
	v_cvt_scalef32_pk_f32_fp4 v[66:67], v0, 1.0 op_sel:[0,1,0]
	v_cvt_scalef32_pk_f32_fp4 v[68:69], v0, 1.0 op_sel:[1,1,0]
	s_nop 0
	v_pk_fma_f32 v[14:15], v[10:11], v[62:63], v[14:15] op_sel_hi:[0,1,1]
	v_pk_fma_f32 v[16:17], v[10:11], v[64:65], v[16:17] op_sel_hi:[0,1,1]
	v_pk_fma_f32 v[18:19], v[10:11], v[66:67], v[18:19] op_sel_hi:[0,1,1]
	v_cvt_scalef32_pk_f32_fp4 v[62:63], v1, 1.0
	v_cvt_scalef32_pk_f32_fp4 v[64:65], v1, 1.0 op_sel:[1,0,0]
	v_cvt_scalef32_pk_f32_fp4 v[66:67], v1, 1.0 op_sel:[0,1,0]
	v_cvt_scalef32_pk_f32_fp4 v[0:1], v1, 1.0 op_sel:[1,1,0]
	v_pk_fma_f32 v[6:7], v[10:11], v[0:1], v[6:7] op_sel_hi:[0,1,1]
	v_cvt_scalef32_pk_f32_fp4 v[0:1], v2, 1.0
	v_pk_fma_f32 v[26:27], v[10:11], v[62:63], v[26:27] op_sel_hi:[0,1,1]
	v_pk_fma_f32 v[30:31], v[10:11], v[64:65], v[30:31] op_sel_hi:[0,1,1]
	v_cvt_scalef32_pk_f32_fp4 v[62:63], v2, 1.0 op_sel:[1,0,0]
	v_cvt_scalef32_pk_f32_fp4 v[64:65], v2, 1.0 op_sel:[0,1,0]
	v_pk_fma_f32 v[58:59], v[10:11], v[0:1], v[58:59] op_sel_hi:[0,1,1]
	v_cvt_scalef32_pk_f32_fp4 v[0:1], v3, 1.0
	v_pk_fma_f32 v[56:57], v[10:11], v[66:67], v[56:57] op_sel_hi:[0,1,1]
	v_cvt_scalef32_pk_f32_fp4 v[66:67], v2, 1.0 op_sel:[1,1,0]
	v_pk_fma_f32 v[28:29], v[10:11], v[62:63], v[28:29] op_sel_hi:[0,1,1]
	v_pk_fma_f32 v[20:21], v[10:11], v[64:65], v[20:21] op_sel_hi:[0,1,1]
	v_cvt_scalef32_pk_f32_fp4 v[62:63], v3, 1.0 op_sel:[1,0,0]
	v_cvt_scalef32_pk_f32_fp4 v[64:65], v3, 1.0 op_sel:[0,1,0]
	v_cvt_scalef32_pk_f32_fp4 v[2:3], v3, 1.0 op_sel:[1,1,0]
	v_pk_fma_f32 v[12:13], v[10:11], v[0:1], v[12:13] op_sel_hi:[0,1,1]
	v_pk_fma_f32 v[24:25], v[10:11], v[68:69], v[24:25] op_sel_hi:[0,1,1]
	v_pk_fma_f32 v[22:23], v[10:11], v[66:67], v[22:23] op_sel_hi:[0,1,1]
	v_pk_fma_f32 v[60:61], v[10:11], v[62:63], v[60:61] op_sel_hi:[0,1,1]
	v_pk_fma_f32 v[4:5], v[10:11], v[64:65], v[4:5] op_sel_hi:[0,1,1]
	v_pk_fma_f32 v[8:9], v[10:11], v[2:3], v[8:9] op_sel_hi:[0,1,1]
	v_mov_b64_e32 v[0:1], v[164:165]
	v_mov_b64_e32 v[2:3], v[166:167]
	s_nop 0
	v_mov_b32_e32 v10, v174
	s_nop 0
	v_cvt_scalef32_pk_f32_fp4 v[62:63], v0, 1.0
	v_cvt_scalef32_pk_f32_fp4 v[64:65], v0, 1.0 op_sel:[1,0,0]
	v_cvt_scalef32_pk_f32_fp4 v[66:67], v0, 1.0 op_sel:[0,1,0]
	v_cvt_scalef32_pk_f32_fp4 v[68:69], v0, 1.0 op_sel:[1,1,0]
	s_nop 0
	v_pk_fma_f32 v[14:15], v[10:11], v[62:63], v[14:15] op_sel_hi:[0,1,1]
	v_pk_fma_f32 v[16:17], v[10:11], v[64:65], v[16:17] op_sel_hi:[0,1,1]
	v_pk_fma_f32 v[18:19], v[10:11], v[66:67], v[18:19] op_sel_hi:[0,1,1]
	v_cvt_scalef32_pk_f32_fp4 v[62:63], v1, 1.0
	v_cvt_scalef32_pk_f32_fp4 v[64:65], v1, 1.0 op_sel:[1,0,0]
	v_cvt_scalef32_pk_f32_fp4 v[66:67], v1, 1.0 op_sel:[0,1,0]
	v_cvt_scalef32_pk_f32_fp4 v[0:1], v1, 1.0 op_sel:[1,1,0]
	v_pk_fma_f32 v[6:7], v[10:11], v[0:1], v[6:7] op_sel_hi:[0,1,1]
	v_cvt_scalef32_pk_f32_fp4 v[0:1], v2, 1.0
	v_pk_fma_f32 v[24:25], v[10:11], v[68:69], v[24:25] op_sel_hi:[0,1,1]
	v_pk_fma_f32 v[68:69], v[10:11], v[66:67], v[56:57] op_sel_hi:[0,1,1]
	v_cvt_scalef32_pk_f32_fp4 v[56:57], v2, 1.0 op_sel:[1,0,0]
	v_pk_fma_f32 v[72:73], v[10:11], v[0:1], v[58:59] op_sel_hi:[0,1,1]
	v_cvt_scalef32_pk_f32_fp4 v[0:1], v3, 1.0
	v_pk_fma_f32 v[26:27], v[10:11], v[62:63], v[26:27] op_sel_hi:[0,1,1]
	v_pk_fma_f32 v[30:31], v[10:11], v[64:65], v[30:31] op_sel_hi:[0,1,1]
	v_cvt_scalef32_pk_f32_fp4 v[62:63], v2, 1.0 op_sel:[0,1,0]
	v_cvt_scalef32_pk_f32_fp4 v[64:65], v2, 1.0 op_sel:[1,1,0]
	v_pk_fma_f32 v[28:29], v[10:11], v[56:57], v[28:29] op_sel_hi:[0,1,1]
	v_cvt_scalef32_pk_f32_fp4 v[56:57], v3, 1.0 op_sel:[1,0,0]
	v_cvt_scalef32_pk_f32_fp4 v[58:59], v3, 1.0 op_sel:[0,1,0]
	v_cvt_scalef32_pk_f32_fp4 v[2:3], v3, 1.0 op_sel:[1,1,0]
	v_pk_fma_f32 v[12:13], v[10:11], v[0:1], v[12:13] op_sel_hi:[0,1,1]
	v_pk_fma_f32 v[20:21], v[10:11], v[62:63], v[20:21] op_sel_hi:[0,1,1]
	v_pk_fma_f32 v[22:23], v[10:11], v[64:65], v[22:23] op_sel_hi:[0,1,1]
	v_pk_fma_f32 v[74:75], v[10:11], v[56:57], v[60:61] op_sel_hi:[0,1,1]
	v_pk_fma_f32 v[4:5], v[10:11], v[58:59], v[4:5] op_sel_hi:[0,1,1]
	v_pk_fma_f32 v[8:9], v[10:11], v[2:3], v[8:9] op_sel_hi:[0,1,1]
	v_mov_b64_e32 v[0:1], v[168:169]
	v_mov_b64_e32 v[2:3], v[170:171]
	s_nop 0
	v_mov_b32_e32 v10, v175
	s_nop 0
	v_cvt_scalef32_pk_f32_fp4 v[56:57], v0, 1.0
	v_cvt_scalef32_pk_f32_fp4 v[58:59], v0, 1.0 op_sel:[1,0,0]
	v_cvt_scalef32_pk_f32_fp4 v[60:61], v0, 1.0 op_sel:[0,1,0]
	v_cvt_scalef32_pk_f32_fp4 v[62:63], v0, 1.0 op_sel:[1,1,0]
	s_nop 0
	v_pk_fma_f32 v[56:57], v[10:11], v[56:57], v[14:15] op_sel_hi:[0,1,1]
	v_pk_fma_f32 v[58:59], v[10:11], v[58:59], v[16:17] op_sel_hi:[0,1,1]
	v_pk_fma_f32 v[60:61], v[10:11], v[60:61], v[18:19] op_sel_hi:[0,1,1]
; __device__ __forceinline__ void row_peer_reduce(const Params& P, unsigned char* ws, int l, int rowi, int lane, float* __restrict__ xout) {
;     ...
;     for (int xb_ = 0; xb_ < 8; ++xb_) { const u4 a = *(const u4*)(PARTQ + ((size_t)xb_ * NTOK + ((n + 5u * (unsigned)xb_) & (size_t)(NTOK - 1))) * 1024u + (unsigned)(16 * lane)); const float psc = PSCL[(size_t)xb_ * NTOK + n];
; #pragma unroll
;         for (int d = 0; d < 4; ++d) { const f2 p0 = __builtin_amdgcn_cvt_scalef32_pk_f32_fp4(a[d], 1.0f, 0), p1 = __builtin_amdgcn_cvt_scalef32_pk_f32_fp4(a[d], 1.0f, 1), p2 = __builtin_amdgcn_cvt_scalef32_pk_f32_fp4(a[d], 1.0f, 2), p3 = __builtin_amdgcn_cvt_scalef32_pk_f32_fp4(a[d], 1.0f, 3);
;             const int o = 16 * (d >> 1) + 8 * (d & 1);
;             acc[o] += psc * p0.x; acc[o + 1] += psc * p0.y; acc[o + 2] += psc * p1.x; acc[o + 3] += psc * p1.y; acc[o + 4] += psc * p2.x; acc[o + 5] += psc * p2.y; acc[o + 6] += psc * p3.x; acc[o + 7] += psc * p3.y; } }
	v_cvt_scalef32_pk_f32_fp4 v[14:15], v1, 1.0
	v_cvt_scalef32_pk_f32_fp4 v[16:17], v1, 1.0 op_sel:[1,0,0]
	v_cvt_scalef32_pk_f32_fp4 v[18:19], v1, 1.0 op_sel:[0,1,0]
	v_cvt_scalef32_pk_f32_fp4 v[0:1], v1, 1.0 op_sel:[1,1,0]
	v_pk_fma_f32 v[64:65], v[10:11], v[14:15], v[26:27] op_sel_hi:[0,1,1]
	v_pk_fma_f32 v[70:71], v[10:11], v[0:1], v[6:7] op_sel_hi:[0,1,1]
	v_cvt_scalef32_pk_f32_fp4 v[0:1], v2, 1.0
	v_cvt_scalef32_pk_f32_fp4 v[6:7], v2, 1.0 op_sel:[1,0,0]
	v_cvt_scalef32_pk_f32_fp4 v[14:15], v2, 1.0 op_sel:[0,1,0]
	v_pk_fma_f32 v[66:67], v[10:11], v[16:17], v[30:31] op_sel_hi:[0,1,1]
	v_cvt_scalef32_pk_f32_fp4 v[16:17], v2, 1.0 op_sel:[1,1,0]
	v_pk_fma_f32 v[72:73], v[10:11], v[0:1], v[72:73] op_sel_hi:[0,1,1]
	v_pk_fma_f32 v[28:29], v[10:11], v[6:7], v[28:29] op_sel_hi:[0,1,1]
	v_pk_fma_f32 v[20:21], v[10:11], v[14:15], v[20:21] op_sel_hi:[0,1,1]
	v_cvt_scalef32_pk_f32_fp4 v[0:1], v3, 1.0
	v_cvt_scalef32_pk_f32_fp4 v[6:7], v3, 1.0 op_sel:[1,0,0]
	v_cvt_scalef32_pk_f32_fp4 v[14:15], v3, 1.0 op_sel:[0,1,0]
	v_cvt_scalef32_pk_f32_fp4 v[2:3], v3, 1.0 op_sel:[1,1,0]
	v_pk_fma_f32 v[62:63], v[10:11], v[62:63], v[24:25] op_sel_hi:[0,1,1]
	v_pk_fma_f32 v[68:69], v[10:11], v[18:19], v[68:69] op_sel_hi:[0,1,1]
	v_pk_fma_f32 v[22:23], v[10:11], v[16:17], v[22:23] op_sel_hi:[0,1,1]
	v_pk_fma_f32 v[12:13], v[10:11], v[0:1], v[12:13] op_sel_hi:[0,1,1]
	v_pk_fma_f32 v[0:1], v[10:11], v[6:7], v[74:75] op_sel_hi:[0,1,1]
	v_pk_fma_f32 v[4:5], v[10:11], v[14:15], v[4:5] op_sel_hi:[0,1,1]
	v_pk_fma_f32 v[2:3], v[10:11], v[2:3], v[8:9] op_sel_hi:[0,1,1]
	s_cbranch_scc0 .LBB0_1593
; __device__ __forceinline__ void row_peer_reduce(const Params& P, unsigned char* ws, int l, int rowi, int lane, float* __restrict__ xout) {
;     ...
;     float s = 0.f;
; #pragma unroll
;     for (int i = 0; i < 32; ++i) s += acc[i];
;     const float mu = wave_sum(s) * (1.f / D); float s2 = 0.f;
; #pragma unroll
;     for (int i = 0; i < 32; ++i) { acc[i] -= mu; s2 += acc[i] * acc[i]; }
;     const float rstd = rsqrtf(wave_sum(s2) * (1.f / D) + LN_EPS);
;     const float* gam = P.in[23] + (size_t)l * D; const float* bet = P.in[24] + (size_t)l * D;
;     bf16* xb = (bf16*)(ws + WS_XB);
; #pragma unroll
;     for (int j = 0; j < 2; ++j) { const int col = 1024 * j + 16 * lane; float o[16];
; #pragma unroll
;         for (int q = 0; q < 4; ++q) { const f4 g4 = *(const f4*)(gam + col + 4 * q), b4 = *(const f4*)(bet + col + 4 * q);
;             o[4 * q] = acc[16 * j + 4 * q] * rstd * g4.x + b4.x; o[4 * q + 1] = acc[16 * j + 4 * q + 1] * rstd * g4.y + b4.y; o[4 * q + 2] = acc[16 * j + 4 * q + 2] * rstd * g4.z + b4.z; o[4 * q + 3] = acc[16 * j + 4 * q + 3] * rstd * g4.w + b4.w;
;             if (xout) *(f4*)(xout + n * D + col + 4 * q) = mk_f4(o[4 * q], o[4 * q + 1], o[4 * q + 2], o[4 * q + 3]); }
	v_add_f32_e32 v6, 0, v56
	v_add_f32_e32 v6, v57, v6
	v_add_f32_e32 v6, v58, v6
	v_add_f32_e32 v6, v59, v6
	v_add_f32_e32 v6, v60, v6
	v_add_f32_e32 v6, v61, v6
	v_add_f32_e32 v6, v62, v6
	v_add_f32_e32 v6, v63, v6
	v_add_f32_e32 v6, v64, v6
	v_add_f32_e32 v6, v65, v6
	v_add_f32_e32 v6, v66, v6
	v_add_f32_e32 v6, v67, v6
	v_add_f32_e32 v6, v68, v6
	v_add_f32_e32 v6, v69, v6
	v_add_f32_e32 v6, v70, v6
	v_add_f32_e32 v6, v71, v6
	v_add_f32_e32 v6, v72, v6
	v_add_f32_e32 v6, v73, v6
	v_add_f32_e32 v6, v28, v6
	v_add_f32_e32 v6, v29, v6
	v_add_f32_e32 v6, v20, v6
	v_add_f32_e32 v6, v21, v6
	v_add_f32_e32 v6, v22, v6
	v_add_f32_e32 v6, v23, v6
	v_add_f32_e32 v6, v12, v6
	v_add_f32_e32 v6, v13, v6
	v_add_f32_e32 v6, v0, v6
	v_add_f32_e32 v6, v1, v6
	v_add_f32_e32 v6, v4, v6
	v_add_f32_e32 v6, v5, v6
	v_add_f32_e32 v6, v2, v6
	v_add_f32_e32 v6, v3, v6
	ds_bpermute_b32 v7, v33, v6
	s_lshl_b64 s[4:5], s[6:7], 13
	s_add_u32 s14, s8, s4
	s_addc_u32 s15, s9, s5
	s_waitcnt lgkmcnt(0)
	v_add_f32_e32 v6, v6, v7
	ds_bpermute_b32 v7, v76, v6
	s_waitcnt lgkmcnt(0)
	v_add_f32_e32 v6, v6, v7
	ds_bpermute_b32 v7, v77, v6
	s_waitcnt lgkmcnt(0)
	v_add_f32_e32 v6, v6, v7
	ds_bpermute_b32 v7, v78, v6
	s_waitcnt lgkmcnt(0)
	v_add_f32_e32 v6, v6, v7
	v_mov_b32_e32 v7, v6
	s_nop 1
	v_permlane16_swap_b32_e32 v6, v7
	v_add_f32_e32 v6, v6, v7
	v_mov_b32_e32 v7, v6
	s_nop 1
	v_permlane32_swap_b32_e32 v6, v7
	v_add_f32_e32 v6, v6, v7
	v_mul_f32_e32 v74, 0x3a000000, v6
	v_pk_add_f32 v[8:9], v[64:65], v[74:75] op_sel_hi:[1,0] neg_lo:[0,1] neg_hi:[0,1]
	v_pk_add_f32 v[10:11], v[66:67], v[74:75] op_sel_hi:[1,0] neg_lo:[0,1] neg_hi:[0,1]
	v_pk_add_f32 v[26:27], v[22:23], v[74:75] op_sel_hi:[1,0] neg_lo:[0,1] neg_hi:[0,1]
	v_pk_add_f32 v[22:23], v[0:1], v[74:75] op_sel_hi:[1,0] neg_lo:[0,1] neg_hi:[0,1]
	v_pk_add_f32 v[18:19], v[2:3], v[74:75] op_sel_hi:[1,0] neg_lo:[0,1] neg_hi:[0,1]
	global_load_dwordx4 v[0:3], v[44:45], off
	global_load_dwordx4 v[64:67], v[46:47], off
	v_pk_add_f32 v[6:7], v[60:61], v[74:75] op_sel_hi:[1,0] neg_lo:[0,1] neg_hi:[0,1]
	v_pk_add_f32 v[62:63], v[62:63], v[74:75] op_sel_hi:[1,0] neg_lo:[0,1] neg_hi:[0,1]
	v_pk_add_f32 v[14:15], v[68:69], v[74:75] op_sel_hi:[1,0] neg_lo:[0,1] neg_hi:[0,1]
	v_pk_add_f32 v[60:61], v[70:71], v[74:75] op_sel_hi:[1,0] neg_lo:[0,1] neg_hi:[0,1]
	v_pk_add_f32 v[30:31], v[72:73], v[74:75] op_sel_hi:[1,0] neg_lo:[0,1] neg_hi:[0,1]
	v_pk_add_f32 v[28:29], v[28:29], v[74:75] op_sel_hi:[1,0] neg_lo:[0,1] neg_hi:[0,1]
	v_pk_add_f32 v[24:25], v[20:21], v[74:75] op_sel_hi:[1,0] neg_lo:[0,1] neg_hi:[0,1]
	v_pk_add_f32 v[20:21], v[12:13], v[74:75] op_sel_hi:[1,0] neg_lo:[0,1] neg_hi:[0,1]
	v_pk_add_f32 v[16:17], v[4:5], v[74:75] op_sel_hi:[1,0] neg_lo:[0,1] neg_hi:[0,1]
	v_pk_add_f32 v[100:101], v[58:59], v[74:75] op_sel_hi:[1,0] neg_lo:[0,1] neg_hi:[0,1]
	v_pk_add_f32 v[74:75], v[56:57], v[74:75] op_sel_hi:[1,0] neg_lo:[0,1] neg_hi:[0,1]
	v_pk_mul_f32 v[58:59], v[100:101], v[100:101]
	v_pk_mul_f32 v[56:57], v[74:75], v[74:75]
	v_pk_mul_f32 v[68:69], v[6:7], v[6:7]
	v_add_f32_e32 v55, v56, v57
	v_add_f32_e32 v55, v58, v55
	v_add_f32_e32 v55, v59, v55
	v_add_f32_e32 v55, v68, v55
	v_pk_mul_f32 v[70:71], v[62:63], v[62:63]
	v_add_f32_e32 v55, v69, v55
	v_add_f32_e32 v55, v70, v55
	v_pk_mul_f32 v[72:73], v[8:9], v[8:9]
	v_add_f32_e32 v55, v71, v55
	v_add_f32_e32 v55, v72, v55
	v_pk_mul_f32 v[82:83], v[10:11], v[10:11]
	v_add_f32_e32 v55, v73, v55
	v_add_f32_e32 v55, v82, v55
	v_pk_mul_f32 v[84:85], v[14:15], v[14:15]
	v_add_f32_e32 v55, v83, v55
	v_add_f32_e32 v55, v84, v55
	v_pk_mul_f32 v[86:87], v[60:61], v[60:61]
	v_add_f32_e32 v55, v85, v55
	v_add_f32_e32 v55, v86, v55
	v_pk_mul_f32 v[88:89], v[30:31], v[30:31]
	v_add_f32_e32 v55, v87, v55
	v_add_f32_e32 v55, v88, v55
	v_pk_mul_f32 v[90:91], v[28:29], v[28:29]
	v_add_f32_e32 v55, v89, v55
	v_add_f32_e32 v55, v90, v55
	v_pk_mul_f32 v[92:93], v[24:25], v[24:25]
	v_add_f32_e32 v55, v91, v55
	v_add_f32_e32 v55, v92, v55
	v_pk_mul_f32 v[94:95], v[26:27], v[26:27]
	v_add_f32_e32 v55, v93, v55
	v_add_f32_e32 v55, v94, v55
	v_pk_mul_f32 v[12:13], v[20:21], v[20:21]
	v_add_f32_e32 v55, v95, v55
	v_add_f32_e32 v12, v12, v55
	v_pk_mul_f32 v[96:97], v[22:23], v[22:23]
	v_add_f32_e32 v12, v13, v12
	v_add_f32_e32 v12, v96, v12
	v_pk_mul_f32 v[4:5], v[16:17], v[16:17]
	v_add_f32_e32 v12, v97, v12
	v_add_f32_e32 v4, v4, v12
	v_pk_mul_f32 v[98:99], v[18:19], v[18:19]
	v_add_f32_e32 v4, v5, v4
	v_add_f32_e32 v4, v98, v4
	v_add_f32_e32 v4, v99, v4
	ds_bpermute_b32 v5, v33, v4
	s_waitcnt lgkmcnt(0)
	v_add_f32_e32 v4, v4, v5
	ds_bpermute_b32 v5, v76, v4
	s_waitcnt lgkmcnt(0)
	v_add_f32_e32 v4, v4, v5
	ds_bpermute_b32 v5, v77, v4
	s_waitcnt lgkmcnt(0)
	v_add_f32_e32 v4, v4, v5
	ds_bpermute_b32 v5, v78, v4
	s_waitcnt lgkmcnt(0)
	v_add_f32_e32 v4, v4, v5
	v_mov_b32_e32 v5, v4
	s_nop 1
	v_permlane16_swap_b32_e32 v4, v5
	v_add_f32_e32 v4, v4, v5
	v_mov_b32_e32 v5, v4
	s_nop 1
	v_permlane32_swap_b32_e32 v4, v5
	v_add_f32_e32 v4, v4, v5
	v_fmamk_f32 v4, v4, 0x3a000000, v194
	v_mul_f32_e32 v5, 0x4b800000, v4
	v_cmp_gt_f32_e32 vcc, s57, v4
	s_nop 1
	v_cndmask_b32_e32 v4, v4, v5, vcc
	v_rsq_f32_e32 v12, v4
	v_lshlrev_b32_e32 v4, 2, v32
	v_mov_b32_e32 v5, v80
	v_lshl_add_u64 v[58:59], s[14:15], 0, v[4:5]
	v_mul_f32_e32 v4, 0x45800000, v12
	v_cndmask_b32_e32 v56, v12, v4, vcc
	v_pk_mul_f32 v[4:5], v[74:75], v[56:57] op_sel_hi:[1,0]
	s_and_b64 vcc, exec, s[10:11]
	s_waitcnt vmcnt(0)
	v_pk_fma_f32 v[0:1], v[0:1], v[4:5], v[64:65]
	v_pk_mul_f32 v[4:5], v[100:101], v[56:57] op_sel_hi:[1,0]
	s_nop 0
	v_pk_fma_f32 v[2:3], v[2:3], v[4:5], v[66:67]
	s_cbranch_vccz .LBB0_1596
	global_store_dwordx4 v[58:59], v[0:3], off

; __device__ __forceinline__ unsigned xb_ld(unsigned* p)              { return __hip_atomic_load(p, __ATOMIC_RELAXED, __HIP_MEMORY_SCOPE_AGENT); }
; __device__ __forceinline__ unsigned xb_add(unsigned* p, unsigned v) { return __hip_atomic_fetch_add(p, v, __ATOMIC_RELAXED, __HIP_MEMORY_SCOPE_AGENT); }
; #define XB_SPIN(cond, bar) do { unsigned _sp = 0; while (cond) { __builtin_amdgcn_s_sleep(1); \
;     if ((++_sp & 255u) == 0u) { if (xb_ld(&(bar)[XB_TMO])) break; if (_sp > XB_SPIN_CAP) { atomicAdd(&(bar)[XB_TMO], 1u); break; } } } } while (0)
; __device__ __forceinline__ void xcd_barrier(const XcdBarrier& b) {
;     ...
;         const unsigned old = xb_add(&bar[XB_XSUB(b.x)], 1u);
;         const unsigned gen = old / nloc;
;         if (old + 1u == (gen + 1u) * nloc) {
;             __builtin_amdgcn_fence(__ATOMIC_RELEASE, "agent");
;             asm volatile("s_waitcnt vmcnt(0)" ::: "memory");
;             const unsigned og = xb_add(&bar[XB_TOP], 1u);
;             const unsigned tg = og / nx;
;             if (og + 1u == (tg + 1u) * nx) xb_add(&bar[XB_TOPGEN], 1u);
;             else XB_SPIN(xb_ld(&bar[XB_TOPGEN]) == tg, bar);
;             __builtin_amdgcn_fence(__ATOMIC_ACQUIRE, "agent");
;             xb_add(&bar[XB_XGEN(b.x)], 1u);
;             asm volatile("s_waitcnt vmcnt(0)" ::: "memory");
;         } else {
;             XB_SPIN(xb_ld(&bar[XB_XGEN(b.x)]) == gen, bar);
.LBB0_1633:
	s_or_b64 exec, exec, s[6:7]
	v_cvt_f32_u32_e32 v4, v2
	s_waitcnt vmcnt(0)
	v_readfirstlane_b32 s6, v3
	v_sub_u32_e32 v3, 0, v2
	v_rcp_iflag_f32_e32 v4, v4
	v_add_u32_e32 v5, s6, v1
	v_mul_f32_e32 v4, 0x4f7ffffe, v4
	v_cvt_u32_f32_e32 v4, v4
	v_mul_lo_u32 v1, v3, v4
	v_mul_hi_u32 v1, v4, v1
	v_add_u32_e32 v1, v4, v1
	v_mul_hi_u32 v1, v5, v1
	v_mul_lo_u32 v3, v1, v2
	v_sub_u32_e32 v3, v5, v3
	v_add_u32_e32 v4, 1, v1
	v_cmp_ge_u32_e32 vcc, v3, v2
	s_nop 1
	v_cndmask_b32_e32 v1, v1, v4, vcc
	v_sub_u32_e32 v4, v3, v2
	v_cndmask_b32_e32 v3, v3, v4, vcc
	v_add_u32_e32 v4, 1, v1
	v_cmp_ge_u32_e32 vcc, v3, v2
	v_add_u32_e32 v3, 1, v5
	s_nop 0
	v_cndmask_b32_e32 v1, v1, v4, vcc
	v_mul_lo_u32 v4, v2, v1
	v_add_u32_e32 v2, v4, v2
	v_cmp_ne_u32_e32 vcc, v3, v2
	s_and_saveexec_b64 s[6:7], vcc
	s_xor_b64 s[6:7], exec, s[6:7]
	s_cbranch_execz .LBB0_1647
	v_readlane_b32 s8, v253, 11
	v_readlane_b32 s9, v253, 12
	s_waitcnt lgkmcnt(0)
	s_nop 3
	global_load_dword v0, v80, s[8:9] sc1
	s_waitcnt vmcnt(0)
	v_cmp_eq_u32_e32 vcc, v0, v1
	s_and_saveexec_b64 s[8:9], vcc
	s_cbranch_execz .LBB0_1646
	s_mov_b32 s22, 1
	s_mov_b64 s[10:11], 0
	s_branch .LBB0_1637

; __device__ __forceinline__ unsigned xb_ld(unsigned* p)              { return __hip_atomic_load(p, __ATOMIC_RELAXED, __HIP_MEMORY_SCOPE_AGENT); }
; #define XB_SPIN(cond, bar) do { unsigned _sp = 0; while (cond) { __builtin_amdgcn_s_sleep(1); \
;     if ((++_sp & 255u) == 0u) { if (xb_ld(&(bar)[XB_TMO])) break; if (_sp > XB_SPIN_CAP) { atomicAdd(&(bar)[XB_TMO], 1u); break; } } } } while (0)
; __device__ __forceinline__ void xcd_barrier(const XcdBarrier& b) {
;     ...
;             XB_SPIN(xb_ld(&bar[XB_XGEN(b.x)]) == gen, bar);
.LBB0_1639:
	v_readlane_b32 s14, v253, 11
	v_readlane_b32 s15, v253, 12
	s_add_i32 s22, s22, 1
	s_mov_b64 s[16:17], -1
	s_nop 2
	global_load_dword v0, v80, s[14:15] sc1
	s_waitcnt vmcnt(0)
	v_cmp_ne_u32_e32 vcc, v0, v1
	s_orn2_b64 s[14:15], vcc, exec
	s_branch .LBB0_1636

; __device__ __forceinline__ unsigned xb_add(unsigned* p, unsigned v) { return __hip_atomic_fetch_add(p, v, __ATOMIC_RELAXED, __HIP_MEMORY_SCOPE_AGENT); }
; __device__ __forceinline__ void xcd_barrier(const XcdBarrier& b) {
;     ...
;             xb_add(&bar[XB_XGEN(b.x)], 1u);
;             asm volatile("s_waitcnt vmcnt(0)" ::: "memory");
.LBB0_1665:
	s_bcnt1_i32_b64 s6, s[6:7]
	v_mov_b32_e32 v0, s6
	v_readlane_b32 s6, v253, 7
	v_readlane_b32 s7, v253, 8
	s_nop 4
	s_nop 0
	s_getpc_b64 s[98:99]
